# baseline (speedup 1.0000x reference)
_Z13logits_kernelPKDv8_DF16bS1_PKfS3_PDv2_fS5_Pf:
	s_load_dwordx4 s[4:7], s[0:1], 0x0
	s_load_dwordx4 s[12:15], s[0:1], 0x10
	s_load_dwordx4 s[24:27], s[0:1], 0x20
	s_load_dwordx2 s[28:29], s[0:1], 0x30
	s_and_b32 s3, s2, 1
	s_lshl_b32 s3, s3, 3
	s_bfe_u32 s10, s2, 0x30003
	s_or_b32 s10, s10, s3
	s_bfe_u32 s3, s2, 0x20001
	s_lshl_b32 s3, s3, 2
	s_lshr_b32 s8, s2, 6
	s_or_b32 s3, s3, s8
	v_lshrrev_b32_e32 v1, 6, v0
	v_and_b32_e32 v2, 63, v0
	s_movk_i32 s11, 0x3000
	v_lshlrev_b32_e32 v2, 4, v2
	v_and_b32_e32 v5, 31, v0
	v_mad_u32_u24 v2, v1, s11, v2
	v_lshlrev_b32_e32 v5, 2, v5
	s_lshl_b32 s9, s3, 9
	v_add_u32_e32 v3, 0x1000, v2
	v_add_u32_e32 v4, 0x2000, v2
	v_add_u32_e32 v5, s9, v5
	s_mul_i32 s8, s10, 0xc000
	s_mul_i32 s9, s3, 0x30000
	s_waitcnt lgkmcnt(0)
	s_load_dword s22, s[14:15], 0x0
	global_load_dword v248, v5, s[12:13]
	global_load_dword v249, v5, s[12:13] offset:128
	global_load_dword v250, v5, s[12:13] offset:256
	global_load_dword v251, v5, s[12:13] offset:384
	s_add_u32 s4, s4, s8
	s_addc_u32 s5, s5, 0
	s_add_u32 s6, s6, s9
	s_addc_u32 s7, s7, 0
	s_add_u32 s16, s6, 0xc000
	s_addc_u32 s17, s7, 0
	s_add_u32 s18, s6, 0x18000
	s_addc_u32 s19, s7, 0
	s_add_u32 s20, s6, 0x24000
	s_addc_u32 s21, s7, 0
	global_load_dwordx4 v[56:59], v2, s[6:7]
	global_load_dwordx4 v[104:107], v2, s[16:17]
	global_load_dwordx4 v[152:155], v2, s[18:19]
	global_load_dwordx4 v[200:203], v2, s[20:21]
	global_load_dwordx4 v[8:11], v2, s[4:5]
	global_load_dwordx4 v[60:63], v2, s[6:7] offset:1024
	global_load_dwordx4 v[108:111], v2, s[16:17] offset:1024
	global_load_dwordx4 v[156:159], v2, s[18:19] offset:1024
	global_load_dwordx4 v[204:207], v2, s[20:21] offset:1024
	global_load_dwordx4 v[12:15], v2, s[4:5] offset:1024
	global_load_dwordx4 v[64:67], v2, s[6:7] offset:2048
	global_load_dwordx4 v[112:115], v2, s[16:17] offset:2048
	global_load_dwordx4 v[160:163], v2, s[18:19] offset:2048
	global_load_dwordx4 v[208:211], v2, s[20:21] offset:2048
	global_load_dwordx4 v[16:19], v2, s[4:5] offset:2048
	global_load_dwordx4 v[68:71], v2, s[6:7] offset:3072
	global_load_dwordx4 v[116:119], v2, s[16:17] offset:3072
	global_load_dwordx4 v[164:167], v2, s[18:19] offset:3072
	global_load_dwordx4 v[212:215], v2, s[20:21] offset:3072
	global_load_dwordx4 v[20:23], v2, s[4:5] offset:3072
	global_load_dwordx4 v[72:75], v3, s[6:7]
	global_load_dwordx4 v[120:123], v3, s[16:17]
	global_load_dwordx4 v[168:171], v3, s[18:19]
	global_load_dwordx4 v[216:219], v3, s[20:21]
	global_load_dwordx4 v[24:27], v3, s[4:5]
	global_load_dwordx4 v[76:79], v3, s[6:7] offset:1024
	global_load_dwordx4 v[124:127], v3, s[16:17] offset:1024
	global_load_dwordx4 v[172:175], v3, s[18:19] offset:1024
	global_load_dwordx4 v[220:223], v3, s[20:21] offset:1024
	global_load_dwordx4 v[28:31], v3, s[4:5] offset:1024
	global_load_dwordx4 v[80:83], v3, s[6:7] offset:2048
	global_load_dwordx4 v[128:131], v3, s[16:17] offset:2048
	global_load_dwordx4 v[176:179], v3, s[18:19] offset:2048
	global_load_dwordx4 v[224:227], v3, s[20:21] offset:2048
	global_load_dwordx4 v[32:35], v3, s[4:5] offset:2048
	global_load_dwordx4 v[84:87], v3, s[6:7] offset:3072
	global_load_dwordx4 v[132:135], v3, s[16:17] offset:3072
	global_load_dwordx4 v[180:183], v3, s[18:19] offset:3072
	global_load_dwordx4 v[228:231], v3, s[20:21] offset:3072
	global_load_dwordx4 v[36:39], v3, s[4:5] offset:3072
	global_load_dwordx4 v[88:91], v4, s[6:7]
	global_load_dwordx4 v[136:139], v4, s[16:17]
	global_load_dwordx4 v[184:187], v4, s[18:19]
	global_load_dwordx4 v[232:235], v4, s[20:21]
	global_load_dwordx4 v[40:43], v4, s[4:5]
	global_load_dwordx4 v[92:95], v4, s[6:7] offset:1024
	global_load_dwordx4 v[140:143], v4, s[16:17] offset:1024
	global_load_dwordx4 v[188:191], v4, s[18:19] offset:1024
	global_load_dwordx4 v[236:239], v4, s[20:21] offset:1024
	global_load_dwordx4 v[44:47], v4, s[4:5] offset:1024
	global_load_dwordx4 v[96:99], v4, s[6:7] offset:2048
	global_load_dwordx4 v[144:147], v4, s[16:17] offset:2048
	global_load_dwordx4 v[192:195], v4, s[18:19] offset:2048
	global_load_dwordx4 v[240:243], v4, s[20:21] offset:2048
	global_load_dwordx4 v[48:51], v4, s[4:5] offset:2048
	global_load_dwordx4 v[100:103], v4, s[6:7] offset:3072
	global_load_dwordx4 v[148:151], v4, s[16:17] offset:3072
	global_load_dwordx4 v[196:199], v4, s[18:19] offset:3072
	global_load_dwordx4 v[244:247], v4, s[20:21] offset:3072
	global_load_dwordx4 v[52:55], v4, s[4:5] offset:3072
	s_waitcnt vmcnt(55)
	v_mfma_f32_32x32x16_bf16 a[0:15], v[8:11], v[56:59], 0
	s_waitcnt vmcnt(55)
	v_mfma_f32_32x32x16_bf16 a[0:15], v[8:11], v[104:107], a[0:15]
	s_waitcnt vmcnt(55)
	v_mfma_f32_32x32x16_bf16 a[0:15], v[8:11], v[152:155], a[0:15]
	s_waitcnt vmcnt(55)
	v_mfma_f32_32x32x16_bf16 a[0:15], v[8:11], v[200:203], a[0:15]
	s_waitcnt vmcnt(50)
	v_mfma_f32_32x32x16_bf16 a[0:15], v[12:15], v[60:63], a[0:15]
	s_waitcnt vmcnt(50)
	v_mfma_f32_32x32x16_bf16 a[0:15], v[12:15], v[108:111], a[0:15]
	s_waitcnt vmcnt(50)
	v_mfma_f32_32x32x16_bf16 a[0:15], v[12:15], v[156:159], a[0:15]
	s_waitcnt vmcnt(50)
	v_mfma_f32_32x32x16_bf16 a[0:15], v[12:15], v[204:207], a[0:15]
	s_waitcnt vmcnt(45)
	v_mfma_f32_32x32x16_bf16 a[0:15], v[16:19], v[64:67], a[0:15]
	s_waitcnt vmcnt(45)
	v_mfma_f32_32x32x16_bf16 a[0:15], v[16:19], v[112:115], a[0:15]
	s_waitcnt vmcnt(45)
	v_mfma_f32_32x32x16_bf16 a[0:15], v[16:19], v[160:163], a[0:15]
	s_waitcnt vmcnt(45)
	v_mfma_f32_32x32x16_bf16 a[0:15], v[16:19], v[208:211], a[0:15]
	s_waitcnt vmcnt(40)
	v_mfma_f32_32x32x16_bf16 a[0:15], v[20:23], v[68:71], a[0:15]
	s_waitcnt vmcnt(40)
	v_mfma_f32_32x32x16_bf16 a[0:15], v[20:23], v[116:119], a[0:15]
	s_waitcnt vmcnt(40)
	v_mfma_f32_32x32x16_bf16 a[0:15], v[20:23], v[164:167], a[0:15]
	s_waitcnt vmcnt(40)
	v_mfma_f32_32x32x16_bf16 a[0:15], v[20:23], v[212:215], a[0:15]
	s_waitcnt vmcnt(35)
	v_mfma_f32_32x32x16_bf16 a[0:15], v[24:27], v[72:75], a[0:15]
	s_waitcnt vmcnt(35)
	v_mfma_f32_32x32x16_bf16 a[0:15], v[24:27], v[120:123], a[0:15]
	s_waitcnt vmcnt(35)
	v_mfma_f32_32x32x16_bf16 a[0:15], v[24:27], v[168:171], a[0:15]
	s_waitcnt vmcnt(35)
	v_mfma_f32_32x32x16_bf16 a[0:15], v[24:27], v[216:219], a[0:15]
	s_waitcnt vmcnt(30)
	v_mfma_f32_32x32x16_bf16 a[0:15], v[28:31], v[76:79], a[0:15]
	s_waitcnt vmcnt(30)
	v_mfma_f32_32x32x16_bf16 a[0:15], v[28:31], v[124:127], a[0:15]
	s_waitcnt vmcnt(30)
	v_mfma_f32_32x32x16_bf16 a[0:15], v[28:31], v[172:175], a[0:15]
	s_waitcnt vmcnt(30)
	v_mfma_f32_32x32x16_bf16 a[0:15], v[28:31], v[220:223], a[0:15]
	s_waitcnt vmcnt(25)
	v_mfma_f32_32x32x16_bf16 a[0:15], v[32:35], v[80:83], a[0:15]
	s_waitcnt vmcnt(25)
	v_mfma_f32_32x32x16_bf16 a[0:15], v[32:35], v[128:131], a[0:15]
	s_waitcnt vmcnt(25)
	v_mfma_f32_32x32x16_bf16 a[0:15], v[32:35], v[176:179], a[0:15]
	s_waitcnt vmcnt(25)
	v_mfma_f32_32x32x16_bf16 a[0:15], v[32:35], v[224:227], a[0:15]
	s_waitcnt vmcnt(20)
	v_mfma_f32_32x32x16_bf16 a[0:15], v[36:39], v[84:87], a[0:15]
	s_waitcnt vmcnt(20)
	v_mfma_f32_32x32x16_bf16 a[0:15], v[36:39], v[132:135], a[0:15]
	s_waitcnt vmcnt(20)
	v_mfma_f32_32x32x16_bf16 a[0:15], v[36:39], v[180:183], a[0:15]
	s_waitcnt vmcnt(20)
	v_mfma_f32_32x32x16_bf16 a[0:15], v[36:39], v[228:231], a[0:15]
	s_waitcnt vmcnt(15)
	v_mfma_f32_32x32x16_bf16 a[0:15], v[40:43], v[88:91], a[0:15]
	s_waitcnt vmcnt(15)
	v_mfma_f32_32x32x16_bf16 a[0:15], v[40:43], v[136:139], a[0:15]
	s_waitcnt vmcnt(15)
	v_mfma_f32_32x32x16_bf16 a[0:15], v[40:43], v[184:187], a[0:15]
	s_waitcnt vmcnt(15)
	v_mfma_f32_32x32x16_bf16 a[0:15], v[40:43], v[232:235], a[0:15]
	s_waitcnt vmcnt(10)
	v_mfma_f32_32x32x16_bf16 a[0:15], v[44:47], v[92:95], a[0:15]
	s_waitcnt vmcnt(10)
	v_mfma_f32_32x32x16_bf16 a[0:15], v[44:47], v[140:143], a[0:15]
	s_waitcnt vmcnt(10)
	v_mfma_f32_32x32x16_bf16 a[0:15], v[44:47], v[188:191], a[0:15]
	s_waitcnt vmcnt(10)
	v_mfma_f32_32x32x16_bf16 a[0:15], v[44:47], v[236:239], a[0:15]
	v_add_f32_e32 v8, 0, v248
	v_add_f32_e32 v8, v8, v249
	v_add_f32_e32 v8, v8, v250
	v_add_f32_e32 v8, v8, v251
	v_mov_b32_e32 v9, 0x3fb8aa3b
	s_waitcnt lgkmcnt(0)
	v_mul_f32_e32 v9, s22, v9
	v_exp_f32_e32 v9, v9
	v_add_f32_e32 v10, 0x2b8cbccc, v8
	v_div_scale_f32 v11, s[8:9], v10, v10, v9
	v_rcp_f32_e32 v12, v11
	v_div_scale_f32 v13, vcc, v9, v10, v9
	v_fma_f32 v14, -v11, v12, 1.0
	v_fmac_f32_e32 v12, v14, v12
	v_mul_f32_e32 v14, v13, v12
	v_fma_f32 v15, -v11, v14, v13
	v_fmac_f32_e32 v14, v15, v12
	v_fma_f32 v11, -v11, v14, v13
	v_div_fmas_f32 v11, v11, v12, v14
	v_div_fixup_f32 v9, v11, v10, v9
	v_lshlrev_b32_e32 v10, 2, v0
	v_add_u32_e32 v10, 0x4000, v10
	v_cmp_gt_u32_e32 vcc, 32, v0
	s_and_saveexec_b64 s[8:9], vcc
	ds_write2_b32 v10, v8, v9 offset0:128 offset1:160
	s_mov_b64 exec, s[8:9]
	s_waitcnt vmcnt(5)
	v_mfma_f32_32x32x16_bf16 a[0:15], v[48:51], v[96:99], a[0:15]
	s_waitcnt vmcnt(5)
	v_mfma_f32_32x32x16_bf16 a[0:15], v[48:51], v[144:147], a[0:15]
	s_waitcnt vmcnt(5)
	v_mfma_f32_32x32x16_bf16 a[0:15], v[48:51], v[192:195], a[0:15]
	s_waitcnt vmcnt(5)
	v_mfma_f32_32x32x16_bf16 a[0:15], v[48:51], v[240:243], a[0:15]
	v_mul_u32_u24_e32 v1, 0x1080, v1
	s_movk_i32 s4, 0x7f
	s_movk_i32 s6, 0x84
	v_cmp_lt_u32_e32 vcc, s4, v0
	v_lshrrev_b32_e32 v11, 3, v0
	v_and_b32_e32 v10, 31, v0
	v_and_b32_e32 v11, 4, v11
	v_mul_u32_u24_e32 v11, 0x84, v11
	v_lshlrev_b32_e32 v9, 2, v10
	v_bfe_u32 v6, v0, 2, 5
	v_and_b32_e32 v7, 3, v0
	v_add3_u32 v1, v1, v11, v9
	v_lshlrev_b32_e32 v8, 3, v7
	s_waitcnt vmcnt(0)
	v_mfma_f32_32x32x16_bf16 a[0:15], v[52:55], v[100:103], a[0:15]
	s_waitcnt vmcnt(0)
	v_mfma_f32_32x32x16_bf16 a[0:15], v[52:55], v[148:151], a[0:15]
	s_waitcnt vmcnt(0)
	v_mfma_f32_32x32x16_bf16 a[0:15], v[52:55], v[196:199], a[0:15]
	s_waitcnt vmcnt(0)
	v_mfma_f32_32x32x16_bf16 a[0:15], v[52:55], v[244:247], a[0:15]
	s_nop 11
	ds_write_b32 v1, a0
	ds_write_b32 v1, a1 offset:132
	ds_write_b32 v1, a2 offset:264
	ds_write_b32 v1, a3 offset:396
	ds_write_b32 v1, a4 offset:1056
	ds_write_b32 v1, a5 offset:1188
	ds_write_b32 v1, a6 offset:1320
	ds_write_b32 v1, a7 offset:1452
	ds_write_b32 v1, a8 offset:2112
	ds_write_b32 v1, a9 offset:2244
	ds_write_b32 v1, a10 offset:2376
	ds_write_b32 v1, a11 offset:2508
	ds_write_b32 v1, a12 offset:3168
	ds_write_b32 v1, a13 offset:3300
	ds_write_b32 v1, a14 offset:3432
	ds_write_b32 v1, a15 offset:3564
	v_bfe_u32 v6, v0, 2, 5
	v_and_b32_e32 v7, 3, v0
	v_lshlrev_b32_e32 v9, 3, v7
	v_readfirstlane_b32 s30, v0
	v_sub_u32_e32 v10, v6, v9
	s_waitcnt lgkmcnt(0)
	s_barrier
	s_cmpk_ge_u32 s30, 0x80
	s_cbranch_scc1 .Llg_k1
	v_mul_u32_u24_e32 v2, 0x84, v6
	v_lshlrev_b32_e32 v8, 5, v7
	v_add_u32_e32 v2, v2, v8
	v_add_u32_e32 v8, 0x4280, v8
	v_add_u32_e32 v3, 0x1080, v2
	v_add_u32_e32 v4, 0x2100, v2
	v_add_u32_e32 v5, 0x3180, v2
	ds_read_b128 v[48:51], v8
	ds_read_b128 v[52:55], v8 offset:16
	ds_read2_b32 v[16:17], v2 offset0:0 offset1:1
	ds_read2_b32 v[18:19], v2 offset0:2 offset1:3
	ds_read2_b32 v[20:21], v2 offset0:4 offset1:5
	ds_read2_b32 v[22:23], v2 offset0:6 offset1:7
	ds_read2_b32 v[24:25], v3 offset0:0 offset1:1
	ds_read2_b32 v[26:27], v3 offset0:2 offset1:3
	ds_read2_b32 v[28:29], v3 offset0:4 offset1:5
	ds_read2_b32 v[30:31], v3 offset0:6 offset1:7
	ds_read2_b32 v[32:33], v4 offset0:0 offset1:1
	ds_read2_b32 v[34:35], v4 offset0:2 offset1:3
	ds_read2_b32 v[36:37], v4 offset0:4 offset1:5
	ds_read2_b32 v[38:39], v4 offset0:6 offset1:7
	s_waitcnt lgkmcnt(4)
	ds_read2_b32 v[40:41], v5 offset0:0 offset1:1
	ds_read2_b32 v[42:43], v5 offset0:2 offset1:3
	ds_read2_b32 v[44:45], v5 offset0:4 offset1:5
	ds_read2_b32 v[46:47], v5 offset0:6 offset1:7
	s_waitcnt lgkmcnt(0)
	s_branch .Llg_join
